# P7 SwiGLU epilogue with packed f32 add/mul (same elementwise f32 ops), scalar-base stores
# speedup vs baseline: 1.0643x; 1.0071x over previous
.LBB0_1152:
	v_lshl_add_u32 v18, s36, 7, v205
	v_ashrrev_i32_e32 v173, 31, v172
	v_lshlrev_b64 v[0:1], 13, v[172:173]
	v_ashrrev_i32_e32 v19, 31, v18
	v_lshl_add_u64 v[2:3], s[12:13], 0, v[0:1]
	v_lshlrev_b64 v[4:5], 2, v[18:19]
	v_lshl_add_u64 v[2:3], v[2:3], 0, v[4:5]
	global_load_dwordx4 v[12:15], v[2:3], off
	v_lshl_add_u64 v[0:1], s[14:15], 0, v[0:1]
	v_lshl_add_u64 v[0:1], v[0:1], 0, v[4:5]
	global_load_dwordx4 v[8:11], v[0:1], off
	global_load_dwordx4 v[4:7], v[2:3], off offset:16
	s_nop 0
	global_load_dwordx4 v[0:3], v[0:1], off offset:16
	v_lshl_add_u32 v20, s55, 8, v179
	s_waitcnt vmcnt(0)
	s_mov_b32 s98, 0x3fd9db23
	s_mov_b32 s100, 0xbfb8aa3b
	v_mov_b32_e32 v30, 1.0
	v_mov_b32_e32 v31, 1.0
	v_lshl_add_u32 v16, v20, 11, v18
	v_pk_add_f32 v[156:157], v[156:157], v[12:13]
	v_min_f32_e32 v156, 0x40e00000, v156
	v_min_f32_e32 v157, 0x40e00000, v157
	v_pk_add_f32 v[158:159], v[158:159], v[14:15]
	v_min_f32_e32 v158, 0x40e00000, v158
	v_min_f32_e32 v159, 0x40e00000, v159
	v_pk_mul_f32 v[18:19], v[156:157], s[98:99] op_sel_hi:[1,0]
	v_pk_mul_f32 v[20:21], v[158:159], s[98:99] op_sel_hi:[1,0]
	v_pk_mul_f32 v[18:19], v[18:19], s[100:101] op_sel_hi:[1,0]
	v_pk_mul_f32 v[20:21], v[20:21], s[100:101] op_sel_hi:[1,0]
	v_exp_f32_e32 v18, v18
	v_exp_f32_e32 v19, v19
	v_exp_f32_e32 v20, v20
	v_exp_f32_e32 v21, v21
	v_pk_add_f32 v[152:153], v[152:153], v[8:9]
	v_pk_add_f32 v[154:155], v[154:155], v[10:11]
	v_pk_add_f32 v[18:19], v[18:19], v[30:31]
	v_pk_add_f32 v[20:21], v[20:21], v[30:31]
	v_rcp_f32_e32 v18, v18
	v_rcp_f32_e32 v19, v19
	v_rcp_f32_e32 v20, v20
	v_rcp_f32_e32 v21, v21
	v_med3_f32 v152, v152, s50, v207
	v_med3_f32 v153, v153, s50, v207
	v_med3_f32 v154, v154, s50, v207
	v_med3_f32 v155, v155, s50, v207
	v_pk_mul_f32 v[156:157], v[156:157], v[18:19]
	v_pk_mul_f32 v[158:159], v[158:159], v[20:21]
	v_pk_add_f32 v[152:153], v[152:153], v[30:31]
	v_pk_add_f32 v[154:155], v[154:155], v[30:31]
	v_pk_mul_f32 v[156:157], v[152:153], v[156:157]
	v_pk_mul_f32 v[158:159], v[154:155], v[158:159]
	v_pk_add_f32 v[148:149], v[148:149], v[4:5]
	v_min_f32_e32 v148, 0x40e00000, v148
	v_min_f32_e32 v149, 0x40e00000, v149
	v_pk_add_f32 v[150:151], v[150:151], v[6:7]
	v_min_f32_e32 v150, 0x40e00000, v150
	v_min_f32_e32 v151, 0x40e00000, v151
	v_pk_mul_f32 v[22:23], v[148:149], s[98:99] op_sel_hi:[1,0]
	v_pk_mul_f32 v[24:25], v[150:151], s[98:99] op_sel_hi:[1,0]
	v_pk_mul_f32 v[22:23], v[22:23], s[100:101] op_sel_hi:[1,0]
	v_pk_mul_f32 v[24:25], v[24:25], s[100:101] op_sel_hi:[1,0]
	v_exp_f32_e32 v22, v22
	v_exp_f32_e32 v23, v23
	v_exp_f32_e32 v24, v24
	v_exp_f32_e32 v25, v25
	v_pk_add_f32 v[144:145], v[144:145], v[0:1]
	v_pk_add_f32 v[146:147], v[146:147], v[2:3]
	v_pk_add_f32 v[22:23], v[22:23], v[30:31]
	v_pk_add_f32 v[24:25], v[24:25], v[30:31]
	v_rcp_f32_e32 v22, v22
	v_rcp_f32_e32 v23, v23
	v_rcp_f32_e32 v24, v24
	v_rcp_f32_e32 v25, v25
	v_med3_f32 v144, v144, s50, v207
	v_med3_f32 v145, v145, s50, v207
	v_med3_f32 v146, v146, s50, v207
	v_med3_f32 v147, v147, s50, v207
	v_pk_mul_f32 v[148:149], v[148:149], v[22:23]
	v_pk_mul_f32 v[150:151], v[150:151], v[24:25]
	v_pk_add_f32 v[144:145], v[144:145], v[30:31]
	v_pk_add_f32 v[146:147], v[146:147], v[30:31]
	v_pk_mul_f32 v[148:149], v[144:145], v[148:149]
	v_pk_mul_f32 v[150:151], v[146:147], v[150:151]
	v_cvt_pk_fp8_f32 v26, v156, v157
	v_cvt_pk_fp8_f32 v27, v148, v149
	v_cvt_pk_fp8_f32 v26, v158, v159 op_sel:[0,0,1]
	v_cvt_pk_fp8_f32 v27, v150, v151 op_sel:[0,0,1]
	v_mov_b32_e32 v17, v16
	s_nop 0
	global_store_dwordx2 v17, v[26:27], s[20:21]
	v_pk_add_f32 v[140:141], v[140:141], v[12:13]
	v_min_f32_e32 v140, 0x40e00000, v140
	v_min_f32_e32 v141, 0x40e00000, v141
	v_pk_add_f32 v[142:143], v[142:143], v[14:15]
	v_min_f32_e32 v142, 0x40e00000, v142
	v_min_f32_e32 v143, 0x40e00000, v143
	v_pk_mul_f32 v[18:19], v[140:141], s[98:99] op_sel_hi:[1,0]
	v_pk_mul_f32 v[20:21], v[142:143], s[98:99] op_sel_hi:[1,0]
	v_pk_mul_f32 v[18:19], v[18:19], s[100:101] op_sel_hi:[1,0]
	v_pk_mul_f32 v[20:21], v[20:21], s[100:101] op_sel_hi:[1,0]
	v_exp_f32_e32 v18, v18
	v_exp_f32_e32 v19, v19
	v_exp_f32_e32 v20, v20
	v_exp_f32_e32 v21, v21
	v_pk_add_f32 v[136:137], v[136:137], v[8:9]
	v_pk_add_f32 v[138:139], v[138:139], v[10:11]
	v_pk_add_f32 v[18:19], v[18:19], v[30:31]
	v_pk_add_f32 v[20:21], v[20:21], v[30:31]
	v_rcp_f32_e32 v18, v18
	v_rcp_f32_e32 v19, v19
	v_rcp_f32_e32 v20, v20
	v_rcp_f32_e32 v21, v21
	v_med3_f32 v136, v136, s50, v207
	v_med3_f32 v137, v137, s50, v207
	v_med3_f32 v138, v138, s50, v207
	v_med3_f32 v139, v139, s50, v207
	v_pk_mul_f32 v[140:141], v[140:141], v[18:19]
	v_pk_mul_f32 v[142:143], v[142:143], v[20:21]
	v_pk_add_f32 v[136:137], v[136:137], v[30:31]
	v_pk_add_f32 v[138:139], v[138:139], v[30:31]
	v_pk_mul_f32 v[140:141], v[136:137], v[140:141]
	v_pk_mul_f32 v[142:143], v[138:139], v[142:143]
	v_pk_add_f32 v[132:133], v[132:133], v[4:5]
	v_min_f32_e32 v132, 0x40e00000, v132
	v_min_f32_e32 v133, 0x40e00000, v133
	v_pk_add_f32 v[134:135], v[134:135], v[6:7]
	v_min_f32_e32 v134, 0x40e00000, v134
	v_min_f32_e32 v135, 0x40e00000, v135
	v_pk_mul_f32 v[22:23], v[132:133], s[98:99] op_sel_hi:[1,0]
	v_pk_mul_f32 v[24:25], v[134:135], s[98:99] op_sel_hi:[1,0]
	v_pk_mul_f32 v[22:23], v[22:23], s[100:101] op_sel_hi:[1,0]
	v_pk_mul_f32 v[24:25], v[24:25], s[100:101] op_sel_hi:[1,0]
	v_exp_f32_e32 v22, v22
	v_exp_f32_e32 v23, v23
	v_exp_f32_e32 v24, v24
	v_exp_f32_e32 v25, v25
	v_pk_add_f32 v[128:129], v[128:129], v[0:1]
	v_pk_add_f32 v[130:131], v[130:131], v[2:3]
	v_pk_add_f32 v[22:23], v[22:23], v[30:31]
	v_pk_add_f32 v[24:25], v[24:25], v[30:31]
	v_rcp_f32_e32 v22, v22
	v_rcp_f32_e32 v23, v23
	v_rcp_f32_e32 v24, v24
	v_rcp_f32_e32 v25, v25
	v_med3_f32 v128, v128, s50, v207
	v_med3_f32 v129, v129, s50, v207
	v_med3_f32 v130, v130, s50, v207
	v_med3_f32 v131, v131, s50, v207
	v_pk_mul_f32 v[132:133], v[132:133], v[22:23]
	v_pk_mul_f32 v[134:135], v[134:135], v[24:25]
	v_pk_add_f32 v[128:129], v[128:129], v[30:31]
	v_pk_add_f32 v[130:131], v[130:131], v[30:31]
	v_pk_mul_f32 v[132:133], v[128:129], v[132:133]
	v_pk_mul_f32 v[134:135], v[130:131], v[134:135]
	v_cvt_pk_fp8_f32 v26, v140, v141
	v_cvt_pk_fp8_f32 v27, v132, v133
	v_cvt_pk_fp8_f32 v26, v142, v143 op_sel:[0,0,1]
	v_cvt_pk_fp8_f32 v27, v134, v135 op_sel:[0,0,1]
	v_add_u32_e32 v17, 0x8000, v16
	s_nop 0
	global_store_dwordx2 v17, v[26:27], s[20:21]
	v_pk_add_f32 v[124:125], v[124:125], v[12:13]
	v_min_f32_e32 v124, 0x40e00000, v124
	v_min_f32_e32 v125, 0x40e00000, v125
	v_pk_add_f32 v[126:127], v[126:127], v[14:15]
	v_min_f32_e32 v126, 0x40e00000, v126
	v_min_f32_e32 v127, 0x40e00000, v127
	v_pk_mul_f32 v[18:19], v[124:125], s[98:99] op_sel_hi:[1,0]
	v_pk_mul_f32 v[20:21], v[126:127], s[98:99] op_sel_hi:[1,0]
	v_pk_mul_f32 v[18:19], v[18:19], s[100:101] op_sel_hi:[1,0]
	v_pk_mul_f32 v[20:21], v[20:21], s[100:101] op_sel_hi:[1,0]
	v_exp_f32_e32 v18, v18
	v_exp_f32_e32 v19, v19
	v_exp_f32_e32 v20, v20
	v_exp_f32_e32 v21, v21
	v_pk_add_f32 v[120:121], v[120:121], v[8:9]
	v_pk_add_f32 v[122:123], v[122:123], v[10:11]
	v_pk_add_f32 v[18:19], v[18:19], v[30:31]
	v_pk_add_f32 v[20:21], v[20:21], v[30:31]
	v_rcp_f32_e32 v18, v18
	v_rcp_f32_e32 v19, v19
	v_rcp_f32_e32 v20, v20
	v_rcp_f32_e32 v21, v21
	v_med3_f32 v120, v120, s50, v207
	v_med3_f32 v121, v121, s50, v207
	v_med3_f32 v122, v122, s50, v207
	v_med3_f32 v123, v123, s50, v207
	v_pk_mul_f32 v[124:125], v[124:125], v[18:19]
	v_pk_mul_f32 v[126:127], v[126:127], v[20:21]
	v_pk_add_f32 v[120:121], v[120:121], v[30:31]
	v_pk_add_f32 v[122:123], v[122:123], v[30:31]
	v_pk_mul_f32 v[124:125], v[120:121], v[124:125]
	v_pk_mul_f32 v[126:127], v[122:123], v[126:127]
	v_pk_add_f32 v[116:117], v[116:117], v[4:5]
	v_min_f32_e32 v116, 0x40e00000, v116
	v_min_f32_e32 v117, 0x40e00000, v117
	v_pk_add_f32 v[118:119], v[118:119], v[6:7]
	v_min_f32_e32 v118, 0x40e00000, v118
	v_min_f32_e32 v119, 0x40e00000, v119
	v_pk_mul_f32 v[22:23], v[116:117], s[98:99] op_sel_hi:[1,0]
	v_pk_mul_f32 v[24:25], v[118:119], s[98:99] op_sel_hi:[1,0]
	v_pk_mul_f32 v[22:23], v[22:23], s[100:101] op_sel_hi:[1,0]
	v_pk_mul_f32 v[24:25], v[24:25], s[100:101] op_sel_hi:[1,0]
	v_exp_f32_e32 v22, v22
	v_exp_f32_e32 v23, v23
	v_exp_f32_e32 v24, v24
	v_exp_f32_e32 v25, v25
	v_pk_add_f32 v[112:113], v[112:113], v[0:1]
	v_pk_add_f32 v[114:115], v[114:115], v[2:3]
	v_pk_add_f32 v[22:23], v[22:23], v[30:31]
	v_pk_add_f32 v[24:25], v[24:25], v[30:31]
	v_rcp_f32_e32 v22, v22
	v_rcp_f32_e32 v23, v23
	v_rcp_f32_e32 v24, v24
	v_rcp_f32_e32 v25, v25
	v_med3_f32 v112, v112, s50, v207
	v_med3_f32 v113, v113, s50, v207
	v_med3_f32 v114, v114, s50, v207
	v_med3_f32 v115, v115, s50, v207
	v_pk_mul_f32 v[116:117], v[116:117], v[22:23]
	v_pk_mul_f32 v[118:119], v[118:119], v[24:25]
	v_pk_add_f32 v[112:113], v[112:113], v[30:31]
	v_pk_add_f32 v[114:115], v[114:115], v[30:31]
	v_pk_mul_f32 v[116:117], v[112:113], v[116:117]
	v_pk_mul_f32 v[118:119], v[114:115], v[118:119]
	v_cvt_pk_fp8_f32 v26, v124, v125
	v_cvt_pk_fp8_f32 v27, v116, v117
	v_cvt_pk_fp8_f32 v26, v126, v127 op_sel:[0,0,1]
	v_cvt_pk_fp8_f32 v27, v118, v119 op_sel:[0,0,1]
	v_add_u32_e32 v17, 0x10000, v16
	s_nop 0
	global_store_dwordx2 v17, v[26:27], s[20:21]
	v_pk_add_f32 v[108:109], v[108:109], v[12:13]
	v_min_f32_e32 v108, 0x40e00000, v108
	v_min_f32_e32 v109, 0x40e00000, v109
	v_pk_add_f32 v[110:111], v[110:111], v[14:15]
	v_min_f32_e32 v110, 0x40e00000, v110
	v_min_f32_e32 v111, 0x40e00000, v111
	v_pk_mul_f32 v[18:19], v[108:109], s[98:99] op_sel_hi:[1,0]
	v_pk_mul_f32 v[20:21], v[110:111], s[98:99] op_sel_hi:[1,0]
	v_pk_mul_f32 v[18:19], v[18:19], s[100:101] op_sel_hi:[1,0]
	v_pk_mul_f32 v[20:21], v[20:21], s[100:101] op_sel_hi:[1,0]
	v_exp_f32_e32 v18, v18
	v_exp_f32_e32 v19, v19
	v_exp_f32_e32 v20, v20
	v_exp_f32_e32 v21, v21
	v_pk_add_f32 v[104:105], v[104:105], v[8:9]
	v_pk_add_f32 v[106:107], v[106:107], v[10:11]
	v_pk_add_f32 v[18:19], v[18:19], v[30:31]
	v_pk_add_f32 v[20:21], v[20:21], v[30:31]
	v_rcp_f32_e32 v18, v18
	v_rcp_f32_e32 v19, v19
	v_rcp_f32_e32 v20, v20
	v_rcp_f32_e32 v21, v21
	v_med3_f32 v104, v104, s50, v207
	v_med3_f32 v105, v105, s50, v207
	v_med3_f32 v106, v106, s50, v207
	v_med3_f32 v107, v107, s50, v207
	v_pk_mul_f32 v[108:109], v[108:109], v[18:19]
	v_pk_mul_f32 v[110:111], v[110:111], v[20:21]
	v_pk_add_f32 v[104:105], v[104:105], v[30:31]
	v_pk_add_f32 v[106:107], v[106:107], v[30:31]
	v_pk_mul_f32 v[108:109], v[104:105], v[108:109]
	v_pk_mul_f32 v[110:111], v[106:107], v[110:111]
	v_pk_add_f32 v[100:101], v[100:101], v[4:5]
	v_min_f32_e32 v100, 0x40e00000, v100
	v_min_f32_e32 v101, 0x40e00000, v101
	v_pk_add_f32 v[102:103], v[102:103], v[6:7]
	v_min_f32_e32 v102, 0x40e00000, v102
	v_min_f32_e32 v103, 0x40e00000, v103
	v_pk_mul_f32 v[22:23], v[100:101], s[98:99] op_sel_hi:[1,0]
	v_pk_mul_f32 v[24:25], v[102:103], s[98:99] op_sel_hi:[1,0]
	v_pk_mul_f32 v[22:23], v[22:23], s[100:101] op_sel_hi:[1,0]
	v_pk_mul_f32 v[24:25], v[24:25], s[100:101] op_sel_hi:[1,0]
	v_exp_f32_e32 v22, v22
	v_exp_f32_e32 v23, v23
	v_exp_f32_e32 v24, v24
	v_exp_f32_e32 v25, v25
	v_pk_add_f32 v[96:97], v[96:97], v[0:1]
	v_pk_add_f32 v[98:99], v[98:99], v[2:3]
	v_pk_add_f32 v[22:23], v[22:23], v[30:31]
	v_pk_add_f32 v[24:25], v[24:25], v[30:31]
	v_rcp_f32_e32 v22, v22
	v_rcp_f32_e32 v23, v23
	v_rcp_f32_e32 v24, v24
	v_rcp_f32_e32 v25, v25
	v_med3_f32 v96, v96, s50, v207
	v_med3_f32 v97, v97, s50, v207
	v_med3_f32 v98, v98, s50, v207
	v_med3_f32 v99, v99, s50, v207
	v_pk_mul_f32 v[100:101], v[100:101], v[22:23]
	v_pk_mul_f32 v[102:103], v[102:103], v[24:25]
	v_pk_add_f32 v[96:97], v[96:97], v[30:31]
	v_pk_add_f32 v[98:99], v[98:99], v[30:31]
	v_pk_mul_f32 v[100:101], v[96:97], v[100:101]
	v_pk_mul_f32 v[102:103], v[98:99], v[102:103]
	v_cvt_pk_fp8_f32 v26, v108, v109
	v_cvt_pk_fp8_f32 v27, v100, v101
	v_cvt_pk_fp8_f32 v26, v110, v111 op_sel:[0,0,1]
	v_cvt_pk_fp8_f32 v27, v102, v103 op_sel:[0,0,1]
	v_add_u32_e32 v17, 0x18000, v16
	s_nop 0
	global_store_dwordx2 v17, v[26:27], s[20:21]
	v_pk_add_f32 v[92:93], v[92:93], v[12:13]
	v_min_f32_e32 v92, 0x40e00000, v92
	v_min_f32_e32 v93, 0x40e00000, v93
	v_pk_add_f32 v[94:95], v[94:95], v[14:15]
	v_min_f32_e32 v94, 0x40e00000, v94
	v_min_f32_e32 v95, 0x40e00000, v95
	v_pk_mul_f32 v[18:19], v[92:93], s[98:99] op_sel_hi:[1,0]
	v_pk_mul_f32 v[20:21], v[94:95], s[98:99] op_sel_hi:[1,0]
	v_pk_mul_f32 v[18:19], v[18:19], s[100:101] op_sel_hi:[1,0]
	v_pk_mul_f32 v[20:21], v[20:21], s[100:101] op_sel_hi:[1,0]
	v_exp_f32_e32 v18, v18
	v_exp_f32_e32 v19, v19
	v_exp_f32_e32 v20, v20
	v_exp_f32_e32 v21, v21
	v_pk_add_f32 v[88:89], v[88:89], v[8:9]
	v_pk_add_f32 v[90:91], v[90:91], v[10:11]
	v_pk_add_f32 v[18:19], v[18:19], v[30:31]
	v_pk_add_f32 v[20:21], v[20:21], v[30:31]
	v_rcp_f32_e32 v18, v18
	v_rcp_f32_e32 v19, v19
	v_rcp_f32_e32 v20, v20
	v_rcp_f32_e32 v21, v21
	v_med3_f32 v88, v88, s50, v207
	v_med3_f32 v89, v89, s50, v207
	v_med3_f32 v90, v90, s50, v207
	v_med3_f32 v91, v91, s50, v207
	v_pk_mul_f32 v[92:93], v[92:93], v[18:19]
	v_pk_mul_f32 v[94:95], v[94:95], v[20:21]
	v_pk_add_f32 v[88:89], v[88:89], v[30:31]
	v_pk_add_f32 v[90:91], v[90:91], v[30:31]
	v_pk_mul_f32 v[92:93], v[88:89], v[92:93]
	v_pk_mul_f32 v[94:95], v[90:91], v[94:95]
	v_pk_add_f32 v[84:85], v[84:85], v[4:5]
	v_min_f32_e32 v84, 0x40e00000, v84
	v_min_f32_e32 v85, 0x40e00000, v85
	v_pk_add_f32 v[86:87], v[86:87], v[6:7]
	v_min_f32_e32 v86, 0x40e00000, v86
	v_min_f32_e32 v87, 0x40e00000, v87
	v_pk_mul_f32 v[22:23], v[84:85], s[98:99] op_sel_hi:[1,0]
	v_pk_mul_f32 v[24:25], v[86:87], s[98:99] op_sel_hi:[1,0]
	v_pk_mul_f32 v[22:23], v[22:23], s[100:101] op_sel_hi:[1,0]
	v_pk_mul_f32 v[24:25], v[24:25], s[100:101] op_sel_hi:[1,0]
	v_exp_f32_e32 v22, v22
	v_exp_f32_e32 v23, v23
	v_exp_f32_e32 v24, v24
	v_exp_f32_e32 v25, v25
	v_pk_add_f32 v[80:81], v[80:81], v[0:1]
	v_pk_add_f32 v[82:83], v[82:83], v[2:3]
	v_pk_add_f32 v[22:23], v[22:23], v[30:31]
	v_pk_add_f32 v[24:25], v[24:25], v[30:31]
	v_rcp_f32_e32 v22, v22
	v_rcp_f32_e32 v23, v23
	v_rcp_f32_e32 v24, v24
	v_rcp_f32_e32 v25, v25
	v_med3_f32 v80, v80, s50, v207
	v_med3_f32 v81, v81, s50, v207
	v_med3_f32 v82, v82, s50, v207
	v_med3_f32 v83, v83, s50, v207
	v_pk_mul_f32 v[84:85], v[84:85], v[22:23]
	v_pk_mul_f32 v[86:87], v[86:87], v[24:25]
	v_pk_add_f32 v[80:81], v[80:81], v[30:31]
	v_pk_add_f32 v[82:83], v[82:83], v[30:31]
	v_pk_mul_f32 v[84:85], v[80:81], v[84:85]
	v_pk_mul_f32 v[86:87], v[82:83], v[86:87]
	v_cvt_pk_fp8_f32 v26, v92, v93
	v_cvt_pk_fp8_f32 v27, v84, v85
	v_cvt_pk_fp8_f32 v26, v94, v95 op_sel:[0,0,1]
	v_cvt_pk_fp8_f32 v27, v86, v87 op_sel:[0,0,1]
	v_add_u32_e32 v17, 0x40000, v16
	s_nop 0
	global_store_dwordx2 v17, v[26:27], s[20:21]
	v_pk_add_f32 v[76:77], v[76:77], v[12:13]
	v_min_f32_e32 v76, 0x40e00000, v76
	v_min_f32_e32 v77, 0x40e00000, v77
	v_pk_add_f32 v[78:79], v[78:79], v[14:15]
	v_min_f32_e32 v78, 0x40e00000, v78
	v_min_f32_e32 v79, 0x40e00000, v79
	v_pk_mul_f32 v[18:19], v[76:77], s[98:99] op_sel_hi:[1,0]
	v_pk_mul_f32 v[20:21], v[78:79], s[98:99] op_sel_hi:[1,0]
	v_pk_mul_f32 v[18:19], v[18:19], s[100:101] op_sel_hi:[1,0]
	v_pk_mul_f32 v[20:21], v[20:21], s[100:101] op_sel_hi:[1,0]
	v_exp_f32_e32 v18, v18
	v_exp_f32_e32 v19, v19
	v_exp_f32_e32 v20, v20
	v_exp_f32_e32 v21, v21
	v_pk_add_f32 v[72:73], v[72:73], v[8:9]
	v_pk_add_f32 v[74:75], v[74:75], v[10:11]
	v_pk_add_f32 v[18:19], v[18:19], v[30:31]
	v_pk_add_f32 v[20:21], v[20:21], v[30:31]
	v_rcp_f32_e32 v18, v18
	v_rcp_f32_e32 v19, v19
	v_rcp_f32_e32 v20, v20
	v_rcp_f32_e32 v21, v21
	v_med3_f32 v72, v72, s50, v207
	v_med3_f32 v73, v73, s50, v207
	v_med3_f32 v74, v74, s50, v207
	v_med3_f32 v75, v75, s50, v207
	v_pk_mul_f32 v[76:77], v[76:77], v[18:19]
	v_pk_mul_f32 v[78:79], v[78:79], v[20:21]
	v_pk_add_f32 v[72:73], v[72:73], v[30:31]
	v_pk_add_f32 v[74:75], v[74:75], v[30:31]
	v_pk_mul_f32 v[76:77], v[72:73], v[76:77]
	v_pk_mul_f32 v[78:79], v[74:75], v[78:79]
	v_pk_add_f32 v[68:69], v[68:69], v[4:5]
	v_min_f32_e32 v68, 0x40e00000, v68
	v_min_f32_e32 v69, 0x40e00000, v69
	v_pk_add_f32 v[70:71], v[70:71], v[6:7]
	v_min_f32_e32 v70, 0x40e00000, v70
	v_min_f32_e32 v71, 0x40e00000, v71
	v_pk_mul_f32 v[22:23], v[68:69], s[98:99] op_sel_hi:[1,0]
	v_pk_mul_f32 v[24:25], v[70:71], s[98:99] op_sel_hi:[1,0]
	v_pk_mul_f32 v[22:23], v[22:23], s[100:101] op_sel_hi:[1,0]
	v_pk_mul_f32 v[24:25], v[24:25], s[100:101] op_sel_hi:[1,0]
	v_exp_f32_e32 v22, v22
	v_exp_f32_e32 v23, v23
	v_exp_f32_e32 v24, v24
	v_exp_f32_e32 v25, v25
	v_pk_add_f32 v[60:61], v[60:61], v[0:1]
	v_pk_add_f32 v[62:63], v[62:63], v[2:3]
	v_pk_add_f32 v[22:23], v[22:23], v[30:31]
	v_pk_add_f32 v[24:25], v[24:25], v[30:31]
	v_rcp_f32_e32 v22, v22
	v_rcp_f32_e32 v23, v23
	v_rcp_f32_e32 v24, v24
	v_rcp_f32_e32 v25, v25
	v_med3_f32 v60, v60, s50, v207
	v_med3_f32 v61, v61, s50, v207
	v_med3_f32 v62, v62, s50, v207
	v_med3_f32 v63, v63, s50, v207
	v_pk_mul_f32 v[68:69], v[68:69], v[22:23]
	v_pk_mul_f32 v[70:71], v[70:71], v[24:25]
	v_pk_add_f32 v[60:61], v[60:61], v[30:31]
	v_pk_add_f32 v[62:63], v[62:63], v[30:31]
	v_pk_mul_f32 v[68:69], v[60:61], v[68:69]
	v_pk_mul_f32 v[70:71], v[62:63], v[70:71]
	v_cvt_pk_fp8_f32 v26, v76, v77
	v_cvt_pk_fp8_f32 v27, v68, v69
	v_cvt_pk_fp8_f32 v26, v78, v79 op_sel:[0,0,1]
	v_cvt_pk_fp8_f32 v27, v70, v71 op_sel:[0,0,1]
	v_add_u32_e32 v17, 0x48000, v16
	s_nop 0
	global_store_dwordx2 v17, v[26:27], s[20:21]
	v_pk_add_f32 v[52:53], v[52:53], v[12:13]
	v_min_f32_e32 v52, 0x40e00000, v52
	v_min_f32_e32 v53, 0x40e00000, v53
	v_pk_add_f32 v[54:55], v[54:55], v[14:15]
	v_min_f32_e32 v54, 0x40e00000, v54
	v_min_f32_e32 v55, 0x40e00000, v55
	v_pk_mul_f32 v[18:19], v[52:53], s[98:99] op_sel_hi:[1,0]
	v_pk_mul_f32 v[20:21], v[54:55], s[98:99] op_sel_hi:[1,0]
	v_pk_mul_f32 v[18:19], v[18:19], s[100:101] op_sel_hi:[1,0]
	v_pk_mul_f32 v[20:21], v[20:21], s[100:101] op_sel_hi:[1,0]
	v_exp_f32_e32 v18, v18
	v_exp_f32_e32 v19, v19
	v_exp_f32_e32 v20, v20
	v_exp_f32_e32 v21, v21
	v_pk_add_f32 v[64:65], v[64:65], v[8:9]
	v_pk_add_f32 v[66:67], v[66:67], v[10:11]
	v_pk_add_f32 v[18:19], v[18:19], v[30:31]
	v_pk_add_f32 v[20:21], v[20:21], v[30:31]
	v_rcp_f32_e32 v18, v18
	v_rcp_f32_e32 v19, v19
	v_rcp_f32_e32 v20, v20
	v_rcp_f32_e32 v21, v21
	v_med3_f32 v64, v64, s50, v207
	v_med3_f32 v65, v65, s50, v207
	v_med3_f32 v66, v66, s50, v207
	v_med3_f32 v67, v67, s50, v207
	v_pk_mul_f32 v[52:53], v[52:53], v[18:19]
	v_pk_mul_f32 v[54:55], v[54:55], v[20:21]
	v_pk_add_f32 v[64:65], v[64:65], v[30:31]
	v_pk_add_f32 v[66:67], v[66:67], v[30:31]
	v_pk_mul_f32 v[52:53], v[64:65], v[52:53]
	v_pk_mul_f32 v[54:55], v[66:67], v[54:55]
	v_pk_add_f32 v[48:49], v[48:49], v[4:5]
	v_min_f32_e32 v48, 0x40e00000, v48
	v_min_f32_e32 v49, 0x40e00000, v49
	v_pk_add_f32 v[50:51], v[50:51], v[6:7]
	v_min_f32_e32 v50, 0x40e00000, v50
	v_min_f32_e32 v51, 0x40e00000, v51
	v_pk_mul_f32 v[22:23], v[48:49], s[98:99] op_sel_hi:[1,0]
	v_pk_mul_f32 v[24:25], v[50:51], s[98:99] op_sel_hi:[1,0]
	v_pk_mul_f32 v[22:23], v[22:23], s[100:101] op_sel_hi:[1,0]
	v_pk_mul_f32 v[24:25], v[24:25], s[100:101] op_sel_hi:[1,0]
	v_exp_f32_e32 v22, v22
	v_exp_f32_e32 v23, v23
	v_exp_f32_e32 v24, v24
	v_exp_f32_e32 v25, v25
	v_pk_add_f32 v[56:57], v[56:57], v[0:1]
	v_pk_add_f32 v[58:59], v[58:59], v[2:3]
	v_pk_add_f32 v[22:23], v[22:23], v[30:31]
	v_pk_add_f32 v[24:25], v[24:25], v[30:31]
	v_rcp_f32_e32 v22, v22
	v_rcp_f32_e32 v23, v23
	v_rcp_f32_e32 v24, v24
	v_rcp_f32_e32 v25, v25
	v_med3_f32 v56, v56, s50, v207
	v_med3_f32 v57, v57, s50, v207
	v_med3_f32 v58, v58, s50, v207
	v_med3_f32 v59, v59, s50, v207
	v_pk_mul_f32 v[48:49], v[48:49], v[22:23]
	v_pk_mul_f32 v[50:51], v[50:51], v[24:25]
	v_pk_add_f32 v[56:57], v[56:57], v[30:31]
	v_pk_add_f32 v[58:59], v[58:59], v[30:31]
	v_pk_mul_f32 v[48:49], v[56:57], v[48:49]
	v_pk_mul_f32 v[50:51], v[58:59], v[50:51]
	v_cvt_pk_fp8_f32 v26, v52, v53
	v_cvt_pk_fp8_f32 v27, v48, v49
	v_cvt_pk_fp8_f32 v26, v54, v55 op_sel:[0,0,1]
	v_cvt_pk_fp8_f32 v27, v50, v51 op_sel:[0,0,1]
	v_add_u32_e32 v17, 0x50000, v16
	s_nop 0
	global_store_dwordx2 v17, v[26:27], s[20:21]
	v_pk_add_f32 v[36:37], v[36:37], v[12:13]
	v_min_f32_e32 v36, 0x40e00000, v36
	v_min_f32_e32 v37, 0x40e00000, v37
	v_pk_add_f32 v[38:39], v[38:39], v[14:15]
	v_min_f32_e32 v38, 0x40e00000, v38
	v_min_f32_e32 v39, 0x40e00000, v39
	v_pk_mul_f32 v[18:19], v[36:37], s[98:99] op_sel_hi:[1,0]
	v_pk_mul_f32 v[20:21], v[38:39], s[98:99] op_sel_hi:[1,0]
	v_pk_mul_f32 v[18:19], v[18:19], s[100:101] op_sel_hi:[1,0]
	v_pk_mul_f32 v[20:21], v[20:21], s[100:101] op_sel_hi:[1,0]
	v_exp_f32_e32 v18, v18
	v_exp_f32_e32 v19, v19
	v_exp_f32_e32 v20, v20
	v_exp_f32_e32 v21, v21
	v_pk_add_f32 v[44:45], v[44:45], v[8:9]
	v_pk_add_f32 v[46:47], v[46:47], v[10:11]
	v_pk_add_f32 v[18:19], v[18:19], v[30:31]
	v_pk_add_f32 v[20:21], v[20:21], v[30:31]
	v_rcp_f32_e32 v18, v18
	v_rcp_f32_e32 v19, v19
	v_rcp_f32_e32 v20, v20
	v_rcp_f32_e32 v21, v21
	v_med3_f32 v44, v44, s50, v207
	v_med3_f32 v45, v45, s50, v207
	v_med3_f32 v46, v46, s50, v207
	v_med3_f32 v47, v47, s50, v207
	v_pk_mul_f32 v[36:37], v[36:37], v[18:19]
	v_pk_mul_f32 v[38:39], v[38:39], v[20:21]
	v_pk_add_f32 v[44:45], v[44:45], v[30:31]
	v_pk_add_f32 v[46:47], v[46:47], v[30:31]
	v_pk_mul_f32 v[36:37], v[44:45], v[36:37]
	v_pk_mul_f32 v[38:39], v[46:47], v[38:39]
	v_pk_add_f32 v[32:33], v[32:33], v[4:5]
	v_min_f32_e32 v32, 0x40e00000, v32
	v_min_f32_e32 v33, 0x40e00000, v33
	v_pk_add_f32 v[34:35], v[34:35], v[6:7]
	v_min_f32_e32 v34, 0x40e00000, v34
	v_min_f32_e32 v35, 0x40e00000, v35
	v_pk_mul_f32 v[22:23], v[32:33], s[98:99] op_sel_hi:[1,0]
	v_pk_mul_f32 v[24:25], v[34:35], s[98:99] op_sel_hi:[1,0]
	v_pk_mul_f32 v[22:23], v[22:23], s[100:101] op_sel_hi:[1,0]
	v_pk_mul_f32 v[24:25], v[24:25], s[100:101] op_sel_hi:[1,0]
	v_exp_f32_e32 v22, v22
	v_exp_f32_e32 v23, v23
	v_exp_f32_e32 v24, v24
	v_exp_f32_e32 v25, v25
	v_pk_add_f32 v[40:41], v[40:41], v[0:1]
	v_pk_add_f32 v[42:43], v[42:43], v[2:3]
	v_pk_add_f32 v[22:23], v[22:23], v[30:31]
	v_pk_add_f32 v[24:25], v[24:25], v[30:31]
	v_rcp_f32_e32 v22, v22
	v_rcp_f32_e32 v23, v23
	v_rcp_f32_e32 v24, v24
	v_rcp_f32_e32 v25, v25
	v_med3_f32 v40, v40, s50, v207
	v_med3_f32 v41, v41, s50, v207
	v_med3_f32 v42, v42, s50, v207
	v_med3_f32 v43, v43, s50, v207
	v_pk_mul_f32 v[32:33], v[32:33], v[22:23]
	v_pk_mul_f32 v[34:35], v[34:35], v[24:25]
	v_pk_add_f32 v[40:41], v[40:41], v[30:31]
	v_pk_add_f32 v[42:43], v[42:43], v[30:31]
	v_pk_mul_f32 v[32:33], v[40:41], v[32:33]
	v_pk_mul_f32 v[34:35], v[42:43], v[34:35]
	v_cvt_pk_fp8_f32 v26, v36, v37
	v_cvt_pk_fp8_f32 v27, v32, v33
	v_cvt_pk_fp8_f32 v26, v38, v39 op_sel:[0,0,1]
	v_cvt_pk_fp8_f32 v27, v34, v35 op_sel:[0,0,1]
	v_add_u32_e32 v17, 0x58000, v16
	s_nop 0
	global_store_dwordx2 v17, v[26:27], s[20:21]
	s_and_b64 vcc, exec, s[4:5]
	s_mov_b64 s[4:5], -1
	s_cbranch_vccnz .LBB0_1143
	s_andn2_b64 vcc, exec, s[18:19]
	s_cbranch_vccnz .LBB0_1142
	s_barrier
	s_branch .LBB0_1142
